# P9 combine+LN2 token loop software-pipelined: next token's loads issued into a second register set before the current token's arithmetic
# baseline (speedup 1.0000x reference)
.LBB0_1148:
	v_readlane_b32 s24, v239, 42
	v_readlane_b32 s28, v239, 46
	v_readlane_b32 s29, v239, 47
	s_cmp_lt_i32 s28, 10
	s_cselect_b64 s[0:1], -1, 0
	s_cmp_gt_i32 s29, 9
	s_cselect_b64 s[2:3], -1, 0
	s_and_b64 s[0:1], s[0:1], s[2:3]
	v_readlane_b32 s25, v239, 43
	v_readlane_b32 s26, v239, 44
	v_readlane_b32 s27, v239, 45
	s_andn2_b64 vcc, exec, s[0:1]
	v_readlane_b32 s30, v239, 48
	v_readlane_b32 s31, v239, 49
	s_cbranch_vccnz .LBB0_1152
	v_readlane_b32 s0, v239, 0
	s_lshr_b32 s0, s0, 6
	v_readlane_b32 s1, v239, 23
	s_add_i32 s2, s0, s1
	v_and_b32_e32 v0, 63, v0
	s_cmp_gt_i32 s2, 0xffff
	s_cbranch_scc1 .LBB0_1152
	v_readlane_b32 s4, v239, 26
	v_lshlrev_b32_e32 v34, 3, v0
	v_readlane_b32 s12, v239, 34
	v_readlane_b32 s13, v239, 35
	v_readlane_b32 s14, v239, 36
	v_readlane_b32 s15, v239, 37
	v_readlane_b32 s16, v239, 38
	v_readlane_b32 s17, v239, 39
	v_ashrrev_i32_e32 v35, 31, v34
	v_readlane_b32 s18, v239, 40
	v_readlane_b32 s19, v239, 41
	s_mov_b64 s[12:13], s[16:17]
	v_lshlrev_b64 v[68:69], 2, v[34:35]
	v_readlane_b32 s5, v239, 27
	v_readlane_b32 s6, v239, 28
	v_readlane_b32 s7, v239, 29
	v_readlane_b32 s8, v239, 30
	v_readlane_b32 s9, v239, 31
	v_readlane_b32 s10, v239, 32
	v_readlane_b32 s11, v239, 33
	s_mov_b64 s[14:15], s[18:19]
	v_lshl_add_u64 v[0:1], s[12:13], 0, v[68:69]
	v_lshl_add_u64 v[2:3], s[14:15], 0, v[68:69]
	v_readlane_b32 s4, v239, 7
	v_readlane_b32 s12, v239, 15
	v_readlane_b32 s13, v239, 16
	v_readlane_b32 s14, v239, 17
	v_readlane_b32 s15, v239, 18
	v_readlane_b32 s16, v239, 19
	v_readlane_b32 s17, v239, 20
	v_readlane_b32 s18, v239, 21
	v_readlane_b32 s19, v239, 22
	s_mov_b64 s[12:13], s[16:17]
	s_mov_b64 s[14:15], s[18:19]
	v_lshl_add_u64 v[32:33], s[12:13], 0, v[68:69]
	global_load_dwordx4 v[38:41], v[0:1], off
	global_load_dwordx4 v[42:45], v[0:1], off offset:16
	global_load_dwordx4 v[46:49], v[2:3], off
	global_load_dwordx4 v[50:53], v[2:3], off offset:16
	global_load_dwordx4 v[54:57], v[0:1], off offset:2048
	global_load_dwordx4 v[58:61], v[0:1], off offset:2064
	global_load_dwordx4 v[62:65], v[2:3], off offset:2048
	global_load_dwordx4 v[70:73], v[2:3], off offset:2064
	v_lshl_add_u64 v[36:37], s[14:15], 0, v[68:69]
	global_load_dwordx4 v[0:3], v[32:33], off offset:16
	global_load_dwordx4 v[4:7], v[32:33], off
	global_load_dwordx4 v[8:11], v[36:37], off offset:16
	global_load_dwordx4 v[12:15], v[36:37], off
	global_load_dwordx4 v[16:19], v[32:33], off offset:2064
	global_load_dwordx4 v[20:23], v[32:33], off offset:2048
	global_load_dwordx4 v[24:27], v[36:37], off offset:2064
	global_load_dwordx4 v[28:31], v[36:37], off offset:2048
	v_mbcnt_lo_u32_b32 v32, -1, 0
	v_readlane_b32 s20, v239, 24
	v_mbcnt_hi_u32_b32 v36, -1, v32
	v_readlane_b32 s21, v239, 25
	v_and_b32_e32 v37, 64, v36
	v_readlane_b32 s5, v239, 8
	v_readlane_b32 s6, v239, 9
	v_readlane_b32 s7, v239, 10
	s_ashr_i32 s3, s2, 31
	s_ashr_i32 s21, s20, 31
	v_xor_b32_e32 v66, 1, v36
	v_add_u32_e32 v37, 64, v37
	s_lshl_b64 s[12:13], s[2:3], 12
	s_lshl_b64 s[4:5], s[20:21], 12
	s_lshl_b64 s[6:7], s[2:3], 4
	v_xor_b32_e32 v67, 2, v36
	v_cmp_lt_i32_e32 vcc, v66, v37
	v_readlane_b32 s8, v239, 11
	v_readlane_b32 s9, v239, 12
	v_xor_b32_e32 v74, 4, v36
	s_add_u32 s14, s6, 0x1400000
	v_cndmask_b32_e32 v66, v36, v66, vcc
	v_cmp_lt_i32_e32 vcc, v67, v37
	v_xor_b32_e32 v75, 8, v36
	s_addc_u32 s15, s7, 0
	s_lshl_b64 s[6:7], s[20:21], 4
	s_lshl_b64 s[8:9], s[2:3], 3
	v_cndmask_b32_e32 v67, v36, v67, vcc
	v_cmp_lt_i32_e32 vcc, v74, v37
	v_readlane_b32 s10, v239, 13
	v_readlane_b32 s11, v239, 14
	v_xor_b32_e32 v76, 16, v36
	v_cndmask_b32_e32 v78, v36, v74, vcc
	v_cmp_lt_i32_e32 vcc, v75, v37
	s_add_u32 s16, s8, 0x3cd00000
	v_xor_b32_e32 v77, 32, v36
	v_cndmask_b32_e32 v79, v36, v75, vcc
	v_cmp_lt_i32_e32 vcc, v76, v37
	s_addc_u32 s17, s9, 0
	s_lshl_b64 s[8:9], s[20:21], 3
	s_lshl_b64 s[18:19], s[2:3], 11
	s_lshl_b64 s[10:11], s[20:21], 11
	v_lshl_add_u64 v[32:33], s[12:13], 0, v[34:35]
	v_cndmask_b32_e32 v80, v36, v76, vcc
	v_cmp_lt_i32_e32 vcc, v77, v37
	s_add_u32 s12, s24, s12
	s_mov_b32 s0, 0x3f9837f0
	v_cndmask_b32_e32 v36, v36, v77, vcc
	s_addc_u32 s13, s25, s13
	v_lshlrev_b32_e32 v74, 2, v66
	v_lshlrev_b32_e32 v75, 2, v67
	v_lshlrev_b32_e32 v77, 2, v79
	v_lshlrev_b32_e32 v79, 2, v36
	v_lshl_add_u64 v[68:69], s[12:13], 0, v[68:69]
	v_lshlrev_b32_e32 v76, 2, v78
	v_lshlrev_b32_e32 v78, 2, v80
	v_lshl_add_u64 v[34:35], v[34:35], 1, s[18:19]
	v_mov_b32_e32 v80, 0
	s_mov_b32 s3, 0xe000000
	s_mov_b32 s18, 0x2a800000
	v_mov_b32_e32 v81, 0x3727c5ac
	s_mov_b32 s19, 0xf800000
	v_mov_b32_e32 v82, 0x260
	s_waitcnt vmcnt(0)
	v_pk_mul_f32 v[46:47], v[46:47], s[0:1] op_sel_hi:[1,0]
	v_pk_mul_f32 v[50:51], v[50:51], s[0:1] op_sel_hi:[1,0]
	v_pk_mul_f32 v[54:55], v[54:55], s[0:1] op_sel_hi:[1,0]
	v_pk_mul_f32 v[36:37], v[40:41], s[0:1] op_sel_hi:[1,0]
	v_pk_mul_f32 v[38:39], v[38:39], s[0:1] op_sel_hi:[1,0]
	v_pk_mul_f32 v[40:41], v[44:45], s[0:1] op_sel_hi:[1,0]
	v_pk_mul_f32 v[42:43], v[42:43], s[0:1] op_sel_hi:[1,0]
	v_pk_mul_f32 v[44:45], v[48:49], s[0:1] op_sel_hi:[1,0]
	v_pk_mul_f32 v[48:49], v[52:53], s[0:1] op_sel_hi:[1,0]
	v_pk_mul_f32 v[52:53], v[56:57], s[0:1] op_sel_hi:[1,0]
	v_pk_mul_f32 v[56:57], v[60:61], s[0:1] op_sel_hi:[1,0]
	v_pk_mul_f32 v[58:59], v[58:59], s[0:1] op_sel_hi:[1,0]
	v_pk_mul_f32 v[60:61], v[64:65], s[0:1] op_sel_hi:[1,0]
	v_pk_mul_f32 v[62:63], v[62:63], s[0:1] op_sel_hi:[1,0]
	v_pk_mul_f32 v[64:65], v[72:73], s[0:1] op_sel_hi:[1,0]
	v_pk_mul_f32 v[66:67], v[70:71], s[0:1] op_sel_hi:[1,0]
	s_mov_b64 s[0:1], 0x800
	v_lshl_add_u64 v[68:69], v[68:69], 0, s[0:1]
	v_lshl_add_u64 v[200:201], s[26:27], 0, v[32:33]
	s_add_u32 s12, s26, s14
	v_lshl_add_u64 v[202:203], s[26:27], 0, v[34:35]
	v_add_co_u32_e64 v200, s[0:1], s18, v200
	s_addc_u32 s13, s27, s15
	v_add_co_u32_e32 v204, vcc, s3, v202
	v_addc_co_u32_e64 v201, s[0:1], 0, v201, s[0:1]
	s_add_u32 s0, s26, s16
	v_addc_co_u32_e32 v205, vcc, 0, v203, vcc
	global_load_dwordx2 v[170:171], v[200:201], off nt
	global_load_dwordx2 v[172:173], v[200:201], off offset:1024 nt
	global_load_dwordx2 v[174:175], v[200:201], off offset:2048 nt
	global_load_dwordx2 v[176:177], v[200:201], off offset:3072 nt
	global_load_dwordx4 v[186:189], v80, s[12:13]
	global_load_dwordx2 v[178:179], v[200:201], off offset:1536 nt
	global_load_dwordx2 v[180:181], v[200:201], off offset:512 nt
	global_load_dwordx2 v[182:183], v[200:201], off offset:3584 nt
	global_load_dwordx2 v[184:185], v[200:201], off offset:2560 nt
	global_load_dwordx4 v[190:193], v[204:205], off nt
	global_load_dwordx4 v[194:197], v[204:205], off offset:1024 nt
	s_addc_u32 s1, s27, s17
	global_load_dwordx2 v[198:199], v80, s[0:1]
	s_add_i32 s2, s2, s20
	s_add_u32 s14, s14, s6
	s_addc_u32 s15, s15, s7
	s_add_u32 s16, s16, s8
	s_addc_u32 s17, s17, s9
	v_lshl_add_u64 v[32:33], v[32:33], 0, s[4:5]
	v_lshl_add_u64 v[34:35], v[34:35], 0, s[10:11]
	s_cmp_lt_i32 s2, 0x10000
	s_cselect_b32 s40, 1, 0
	s_waitcnt vmcnt(0)
	s_branch .Lp9_entry
.LBB0_1151:
	s_waitcnt vmcnt(4)
.Lp9_entry:
	v_mov_b32_e32 v94, v170
	v_mov_b32_e32 v95, v171
	v_mov_b32_e32 v96, v172
	v_mov_b32_e32 v97, v173
	v_mov_b32_e32 v98, v174
	v_mov_b32_e32 v99, v175
	v_mov_b32_e32 v100, v176
	v_mov_b32_e32 v101, v177
	v_mov_b32_e32 v102, v178
	v_mov_b32_e32 v103, v179
	v_mov_b32_e32 v104, v180
	v_mov_b32_e32 v105, v181
	v_mov_b32_e32 v106, v182
	v_mov_b32_e32 v107, v183
	v_mov_b32_e32 v108, v184
	v_mov_b32_e32 v109, v185
	v_mov_b32_e32 v84, v186
	v_mov_b32_e32 v85, v187
	v_mov_b32_e32 v86, v188
	v_mov_b32_e32 v87, v189
	v_mov_b32_e32 v70, v190
	v_mov_b32_e32 v71, v191
	v_mov_b32_e32 v72, v192
	v_mov_b32_e32 v73, v193
	v_mov_b32_e32 v88, v194
	v_mov_b32_e32 v89, v195
	v_mov_b32_e32 v90, v196
	v_mov_b32_e32 v91, v197
	v_mov_b32_e32 v92, v198
	v_mov_b32_e32 v93, v199
	s_mov_b32 s41, s40
	s_cmp_eq_u32 s40, 0
	s_cbranch_scc1 .Lp9_nopf
	v_lshl_add_u64 v[200:201], s[26:27], 0, v[32:33]
	s_add_u32 s12, s26, s14
	v_lshl_add_u64 v[202:203], s[26:27], 0, v[34:35]
	v_add_co_u32_e64 v200, s[0:1], s18, v200
	s_addc_u32 s13, s27, s15
	v_add_co_u32_e32 v204, vcc, s3, v202
	v_addc_co_u32_e64 v201, s[0:1], 0, v201, s[0:1]
	s_add_u32 s0, s26, s16
	v_addc_co_u32_e32 v205, vcc, 0, v203, vcc
	global_load_dwordx2 v[170:171], v[200:201], off nt
	global_load_dwordx2 v[172:173], v[200:201], off offset:1024 nt
	global_load_dwordx2 v[174:175], v[200:201], off offset:2048 nt
	global_load_dwordx2 v[176:177], v[200:201], off offset:3072 nt
	global_load_dwordx4 v[186:189], v80, s[12:13]
	global_load_dwordx2 v[178:179], v[200:201], off offset:1536 nt
	global_load_dwordx2 v[180:181], v[200:201], off offset:512 nt
	global_load_dwordx2 v[182:183], v[200:201], off offset:3584 nt
	global_load_dwordx2 v[184:185], v[200:201], off offset:2560 nt
	global_load_dwordx4 v[190:193], v[204:205], off nt
	global_load_dwordx4 v[194:197], v[204:205], off offset:1024 nt
	s_addc_u32 s1, s27, s17
	global_load_dwordx2 v[198:199], v80, s[0:1]
	s_add_i32 s2, s2, s20
	s_add_u32 s14, s14, s6
	s_addc_u32 s15, s15, s7
	s_add_u32 s16, s16, s8
	s_addc_u32 s17, s17, s9
	v_lshl_add_u64 v[32:33], v[32:33], 0, s[4:5]
	v_lshl_add_u64 v[34:35], v[34:35], 0, s[10:11]
	s_cmp_lt_i32 s2, 0x10000
	s_cselect_b32 s40, 1, 0
.Lp9_nopf:
	v_cvt_pk_f32_fp8_e32 v[110:111], v94
	v_cvt_pk_f32_fp8_sdwa v[112:113], v94 src0_sel:WORD_1
	v_cvt_pk_f32_fp8_e32 v[114:115], v95
	v_cvt_pk_f32_fp8_sdwa v[94:95], v95 src0_sel:WORD_1
	v_cvt_pk_f32_fp8_e32 v[116:117], v96
	v_cvt_pk_f32_fp8_sdwa v[118:119], v96 src0_sel:WORD_1
	v_cvt_pk_f32_fp8_e32 v[136:137], v104
	v_cvt_pk_f32_fp8_sdwa v[138:139], v104 src0_sel:WORD_1
	v_cvt_pk_f32_fp8_e32 v[140:141], v105
	v_cvt_pk_f32_fp8_sdwa v[104:105], v105 src0_sel:WORD_1
	v_cvt_pk_f32_fp8_e32 v[142:143], v102
	v_cvt_pk_f32_fp8_sdwa v[144:145], v102 src0_sel:WORD_1
	v_lshlrev_b32_e32 v160, 16, v70
	v_and_b32_e32 v161, 0xffff0000, v70
	v_lshlrev_b32_e32 v70, 16, v71
	v_and_b32_e32 v71, 0xffff0000, v71
	v_lshlrev_b32_e32 v162, 16, v72
	v_and_b32_e32 v163, 0xffff0000, v72
	v_lshlrev_b32_e32 v72, 16, v73
	v_and_b32_e32 v73, 0xffff0000, v73
	v_lshlrev_b32_e32 v164, 16, v88
	v_and_b32_e32 v165, 0xffff0000, v88
	v_lshlrev_b32_e32 v88, 16, v89
	v_and_b32_e32 v89, 0xffff0000, v89
	v_cvt_pk_f32_fp8_e32 v[120:121], v97
	v_cvt_pk_f32_fp8_sdwa v[96:97], v97 src0_sel:WORD_1
	v_cvt_pk_f32_fp8_e32 v[122:123], v98
	v_cvt_pk_f32_fp8_sdwa v[124:125], v98 src0_sel:WORD_1
	v_cvt_pk_f32_fp8_e32 v[146:147], v103
	v_cvt_pk_f32_fp8_sdwa v[102:103], v103 src0_sel:WORD_1
	v_cvt_pk_f32_fp8_e32 v[148:149], v108
	v_cvt_pk_f32_fp8_sdwa v[150:151], v108 src0_sel:WORD_1
	v_lshlrev_b32_e32 v166, 16, v90
	v_and_b32_e32 v167, 0xffff0000, v90
	v_lshlrev_b32_e32 v90, 16, v91
	v_and_b32_e32 v91, 0xffff0000, v91
	v_pk_fma_f32 v[160:161], v[92:93], v[160:161], v[92:93] op_sel:[0,0,1] op_sel_hi:[0,1,1]
	v_pk_fma_f32 v[70:71], v[92:93], v[70:71], v[92:93] op_sel:[0,0,1] op_sel_hi:[0,1,1]
	v_pk_fma_f32 v[162:163], v[92:93], v[162:163], v[92:93] op_sel:[0,0,1] op_sel_hi:[0,1,1]
	v_pk_fma_f32 v[72:73], v[92:93], v[72:73], v[92:93] op_sel:[0,0,1] op_sel_hi:[0,1,1]
	v_pk_fma_f32 v[164:165], v[92:93], v[164:165], v[92:93] op_sel:[0,0,1] op_sel_hi:[0,1,1]
	v_pk_fma_f32 v[88:89], v[92:93], v[88:89], v[92:93] op_sel:[0,0,1] op_sel_hi:[0,1,1]
	v_cvt_pk_f32_fp8_e32 v[126:127], v99
	v_cvt_pk_f32_fp8_sdwa v[98:99], v99 src0_sel:WORD_1
	v_cvt_pk_f32_fp8_e32 v[128:129], v100
	v_cvt_pk_f32_fp8_sdwa v[130:131], v100 src0_sel:WORD_1
	v_cvt_pk_f32_fp8_e32 v[152:153], v109
	v_cvt_pk_f32_fp8_sdwa v[108:109], v109 src0_sel:WORD_1
	v_cvt_pk_f32_fp8_e32 v[154:155], v106
	v_cvt_pk_f32_fp8_sdwa v[156:157], v106 src0_sel:WORD_1
	v_pk_fma_f32 v[166:167], v[92:93], v[166:167], v[92:93] op_sel:[0,0,1] op_sel_hi:[0,1,1]
	v_pk_fma_f32 v[90:91], v[92:93], v[90:91], v[92:93] op_sel:[0,0,1] op_sel_hi:[0,1,1]
	v_pk_fma_f32 v[70:71], v[36:37], v[70:71], v[44:45]
	v_pk_fma_f32 v[92:93], v[38:39], v[160:161], v[46:47]
	v_pk_fma_f32 v[72:73], v[40:41], v[72:73], v[48:49]
	v_pk_fma_f32 v[160:161], v[42:43], v[162:163], v[50:51]
	v_pk_fma_f32 v[88:89], v[52:53], v[88:89], v[60:61]
	v_pk_fma_f32 v[162:163], v[54:55], v[164:165], v[62:63]
	v_cvt_pk_f32_fp8_e32 v[132:133], v101
	v_cvt_pk_f32_fp8_sdwa v[134:135], v101 src0_sel:WORD_1
	v_cvt_pk_f32_fp8_e32 v[158:159], v107
	v_cvt_pk_f32_fp8_sdwa v[106:107], v107 src0_sel:WORD_1
	v_pk_fma_f32 v[90:91], v[56:57], v[90:91], v[64:65]
	v_pk_fma_f32 v[164:165], v[58:59], v[166:167], v[66:67]
	v_pk_fma_f32 v[92:93], v[84:85], v[110:111], v[92:93] op_sel_hi:[0,1,1]
	v_pk_fma_f32 v[70:71], v[84:85], v[112:113], v[70:71] op_sel_hi:[0,1,1]
	v_pk_fma_f32 v[72:73], v[84:85], v[94:95], v[72:73] op_sel_hi:[0,1,1]
	v_pk_fma_f32 v[94:95], v[84:85], v[136:137], v[162:163] op_sel_hi:[0,1,1]
	v_pk_fma_f32 v[88:89], v[84:85], v[138:139], v[88:89] op_sel_hi:[0,1,1]
	v_pk_fma_f32 v[110:111], v[84:85], v[114:115], v[160:161] op_sel_hi:[0,1,1]
	v_pk_fma_f32 v[112:113], v[84:85], v[140:141], v[164:165] op_sel_hi:[0,1,1]
	v_pk_fma_f32 v[90:91], v[84:85], v[104:105], v[90:91] op_sel_hi:[0,1,1]
	v_pk_fma_f32 v[70:71], v[84:85], v[118:119], v[70:71] op_sel:[1,0,0]
	v_pk_fma_f32 v[92:93], v[84:85], v[116:117], v[92:93] op_sel:[1,0,0]
	v_pk_fma_f32 v[88:89], v[84:85], v[144:145], v[88:89] op_sel:[1,0,0]
	v_pk_fma_f32 v[94:95], v[84:85], v[142:143], v[94:95] op_sel:[1,0,0]
	v_mov_b32_e32 v100, v87
	v_pk_fma_f32 v[72:73], v[84:85], v[96:97], v[72:73] op_sel:[1,0,0]
	v_pk_fma_f32 v[96:97], v[84:85], v[120:121], v[110:111] op_sel:[1,0,0]
	v_pk_fma_f32 v[90:91], v[84:85], v[102:103], v[90:91] op_sel:[1,0,0]
	v_pk_fma_f32 v[84:85], v[84:85], v[146:147], v[112:113] op_sel:[1,0,0]
	v_pk_fma_f32 v[92:93], v[86:87], v[122:123], v[92:93] op_sel_hi:[0,1,1]
	v_pk_fma_f32 v[70:71], v[86:87], v[124:125], v[70:71] op_sel_hi:[0,1,1]
	v_pk_fma_f32 v[94:95], v[86:87], v[148:149], v[94:95] op_sel_hi:[0,1,1]
	v_pk_fma_f32 v[88:89], v[86:87], v[150:151], v[88:89] op_sel_hi:[0,1,1]
	v_pk_fma_f32 v[96:97], v[86:87], v[126:127], v[96:97] op_sel_hi:[0,1,1]
	v_pk_fma_f32 v[72:73], v[86:87], v[98:99], v[72:73] op_sel_hi:[0,1,1]
	v_pk_fma_f32 v[84:85], v[86:87], v[152:153], v[84:85] op_sel_hi:[0,1,1]
	v_pk_fma_f32 v[86:87], v[86:87], v[108:109], v[90:91] op_sel_hi:[0,1,1]
	v_pk_fma_f32 v[70:71], v[100:101], v[130:131], v[70:71] op_sel_hi:[0,1,1]
	v_pk_fma_f32 v[90:91], v[100:101], v[128:129], v[92:93] op_sel_hi:[0,1,1]
	v_pk_fma_f32 v[88:89], v[100:101], v[156:157], v[88:89] op_sel_hi:[0,1,1]
	v_pk_fma_f32 v[94:95], v[100:101], v[154:155], v[94:95] op_sel_hi:[0,1,1]
	v_pk_fma_f32 v[72:73], v[100:101], v[134:135], v[72:73] op_sel_hi:[0,1,1]
	v_pk_fma_f32 v[92:93], v[100:101], v[132:133], v[96:97] op_sel_hi:[0,1,1]
	v_pk_fma_f32 v[86:87], v[100:101], v[106:107], v[86:87] op_sel_hi:[0,1,1]
	v_pk_fma_f32 v[84:85], v[100:101], v[158:159], v[84:85] op_sel_hi:[0,1,1]
	v_mov_b32_e32 v96, v90
	v_mov_b32_e32 v97, v94
	v_mov_b32_e32 v98, v91
	v_mov_b32_e32 v99, v95
	v_mov_b32_e32 v100, v70
	v_mov_b32_e32 v101, v88
	v_mov_b32_e32 v102, v71
	v_mov_b32_e32 v103, v89
	v_mov_b32_e32 v104, v92
	v_mov_b32_e32 v105, v84
	v_mov_b32_e32 v106, v93
	v_mov_b32_e32 v107, v85
	v_pk_add_f32 v[96:97], v[96:97], v[98:99]
	v_pk_add_f32 v[98:99], v[100:101], v[102:103]
	v_mov_b32_e32 v108, v72
	v_mov_b32_e32 v109, v86
	v_mov_b32_e32 v110, v73
	v_mov_b32_e32 v111, v87
	v_pk_add_f32 v[100:101], v[104:105], v[106:107]
	v_pk_add_f32 v[96:97], v[96:97], v[98:99]
	v_pk_add_f32 v[102:103], v[108:109], v[110:111]
	v_pk_add_f32 v[96:97], v[96:97], v[100:101]
	s_nop 0
	v_pk_add_f32 v[96:97], v[102:103], v[96:97]
	s_nop 0
	v_add_f32_e32 v83, 0, v96
	v_add_f32_e32 v83, v83, v97
	ds_bpermute_b32 v96, v74, v83
	s_waitcnt lgkmcnt(0)
	v_add_f32_e32 v83, v83, v96
	ds_bpermute_b32 v96, v75, v83
	s_waitcnt lgkmcnt(0)
	v_add_f32_e32 v83, v83, v96
	ds_bpermute_b32 v96, v76, v83
	s_waitcnt lgkmcnt(0)
	v_add_f32_e32 v83, v83, v96
	ds_bpermute_b32 v96, v77, v83
	s_waitcnt lgkmcnt(0)
	v_add_f32_e32 v83, v83, v96
	ds_bpermute_b32 v96, v78, v83
	s_waitcnt lgkmcnt(0)
	v_add_f32_e32 v83, v83, v96
	ds_bpermute_b32 v96, v79, v83
	s_waitcnt lgkmcnt(0)
	v_add_f32_e32 v83, v83, v96
	v_fmamk_f32 v91, v83, 0xba800000, v91
	v_fmac_f32_e32 v90, 0xba800000, v83
	v_fmamk_f32 v71, v83, 0xba800000, v71
	v_fmac_f32_e32 v70, 0xba800000, v83
	v_fmamk_f32 v93, v83, 0xba800000, v93
	v_fmac_f32_e32 v92, 0xba800000, v83
	v_fmamk_f32 v73, v83, 0xba800000, v73
	v_fmac_f32_e32 v72, 0xba800000, v83
	v_pk_mul_f32 v[96:97], v[70:71], v[70:71]
	v_pk_mul_f32 v[98:99], v[90:91], v[90:91]
	v_pk_mul_f32 v[100:101], v[72:73], v[72:73]
	v_pk_mul_f32 v[102:103], v[92:93], v[92:93]
	v_fmamk_f32 v95, v83, 0xba800000, v95
	v_fmamk_f32 v89, v83, 0xba800000, v89
	v_fmamk_f32 v85, v83, 0xba800000, v85
	v_pk_mov_b32 v[108:109], v[98:99], v[96:97] op_sel:[1,0]
	v_mov_b32_e32 v99, v97
	v_pk_mov_b32 v[96:97], v[102:103], v[100:101] op_sel:[1,0]
	v_mov_b32_e32 v103, v101
	v_fmac_f32_e32 v94, 0xba800000, v83
	v_fmac_f32_e32 v88, 0xba800000, v83
	v_fmamk_f32 v87, v83, 0xba800000, v87
	v_fmac_f32_e32 v86, 0xba800000, v83
	v_fmac_f32_e32 v84, 0xba800000, v83
	v_mul_f32_e32 v107, v85, v85
	v_mul_f32_e32 v104, v95, v95
	v_mul_f32_e32 v106, v89, v89
	v_pk_add_f32 v[98:99], v[108:109], v[98:99]
	v_pk_add_f32 v[96:97], v[96:97], v[102:103]
	v_mul_f32_e32 v83, v84, v84
	v_mul_f32_e32 v110, v86, v86
	v_mul_f32_e32 v111, v87, v87
	v_pk_fma_f32 v[100:101], v[94:95], v[94:95], v[104:105] op_sel_hi:[1,1,0]
	v_pk_fma_f32 v[104:105], v[88:89], v[88:89], v[106:107] op_sel_hi:[1,1,0]
	v_pk_add_f32 v[98:99], v[98:99], v[98:99] op_sel:[0,1] op_sel_hi:[1,0]
	v_pk_add_f32 v[96:97], v[96:97], v[96:97] op_sel:[0,1] op_sel_hi:[1,0]
	v_mov_b32_e32 v101, v110
	v_mov_b32_e32 v105, v111
	v_mov_b32_e32 v99, v83
	v_mov_b32_e32 v97, v107
	v_pk_add_f32 v[100:101], v[100:101], v[104:105]
	v_pk_add_f32 v[96:97], v[98:99], v[96:97]
	s_nop 0
	v_pk_add_f32 v[96:97], v[96:97], v[100:101]
	s_nop 0
	v_add_f32_e32 v83, v96, v97
	ds_bpermute_b32 v96, v74, v83
	s_waitcnt lgkmcnt(0)
	v_add_f32_e32 v83, v83, v96
	ds_bpermute_b32 v96, v75, v83
	s_waitcnt lgkmcnt(0)
	v_add_f32_e32 v83, v83, v96
	ds_bpermute_b32 v96, v76, v83
	s_waitcnt lgkmcnt(0)
	v_add_f32_e32 v83, v83, v96
	ds_bpermute_b32 v96, v77, v83
	s_waitcnt lgkmcnt(0)
	v_add_f32_e32 v83, v83, v96
	ds_bpermute_b32 v96, v78, v83
	s_waitcnt lgkmcnt(0)
	v_add_f32_e32 v83, v83, v96
	ds_bpermute_b32 v96, v79, v83
	s_waitcnt lgkmcnt(0)
	v_add_f32_e32 v83, v83, v96
	v_fmamk_f32 v83, v83, 0x3a800000, v81
	v_mul_f32_e32 v96, 0x4f800000, v83
	v_cmp_gt_f32_e32 vcc, s19, v83
	s_nop 1
	v_cndmask_b32_e32 v83, v83, v96, vcc
	v_sqrt_f32_e32 v96, v83
	s_nop 0
	v_add_u32_e32 v97, -1, v96
	v_add_u32_e32 v98, 1, v96
	v_fma_f32 v99, -v97, v96, v83
	v_fma_f32 v100, -v98, v96, v83
	v_cmp_ge_f32_e64 s[0:1], 0, v99
	s_nop 1
	v_cndmask_b32_e64 v96, v96, v97, s[0:1]
	v_cmp_lt_f32_e64 s[0:1], 0, v100
	s_nop 1
	v_cndmask_b32_e64 v96, v96, v98, s[0:1]
	v_mul_f32_e32 v97, 0x37800000, v96
	v_cndmask_b32_e32 v96, v96, v97, vcc
	v_cmp_class_f32_e32 vcc, v83, v82
	s_nop 1
	v_cndmask_b32_e32 v83, v96, v83, vcc
	v_div_scale_f32 v96, s[0:1], v83, v83, 1.0
	v_rcp_f32_e32 v98, v96
	v_div_scale_f32 v97, vcc, 1.0, v83, 1.0
	v_fma_f32 v99, -v96, v98, 1.0
	v_fmac_f32_e32 v98, v99, v98
	v_mul_f32_e32 v99, v97, v98
	v_fma_f32 v100, -v96, v99, v97
	v_fmac_f32_e32 v99, v100, v98
	v_fma_f32 v96, -v96, v99, v97
	v_div_fmas_f32 v96, v96, v98, v99
	v_div_fixup_f32 v96, v96, v83, 1.0
	v_pk_mul_f32 v[90:91], v[96:97], v[90:91] op_sel_hi:[0,1]
	v_pk_mul_f32 v[70:71], v[96:97], v[70:71] op_sel_hi:[0,1]
	v_pk_mul_f32 v[92:93], v[96:97], v[92:93] op_sel_hi:[0,1]
	v_pk_mul_f32 v[98:99], v[96:97], v[72:73] op_sel_hi:[0,1]
	v_pk_mul_f32 v[94:95], v[96:97], v[94:95] op_sel_hi:[0,1]
	v_pk_mul_f32 v[88:89], v[96:97], v[88:89] op_sel_hi:[0,1]
	v_pk_mul_f32 v[100:101], v[96:97], v[84:85] op_sel_hi:[0,1]
	v_pk_mul_f32 v[96:97], v[96:97], v[86:87] op_sel_hi:[0,1]
	v_pk_fma_f32 v[72:73], v[70:71], v[6:7], v[14:15]
	v_pk_fma_f32 v[70:71], v[90:91], v[4:5], v[12:13]
	v_pk_fma_f32 v[86:87], v[98:99], v[2:3], v[10:11]
	v_pk_fma_f32 v[84:85], v[92:93], v[0:1], v[8:9]
	v_pk_fma_f32 v[90:91], v[88:89], v[22:23], v[30:31]
	v_pk_fma_f32 v[88:89], v[94:95], v[20:21], v[28:29]
	v_pk_fma_f32 v[94:95], v[96:97], v[18:19], v[26:27]
	v_pk_fma_f32 v[92:93], v[100:101], v[16:17], v[24:25]
	global_store_dwordx4 v[68:69], v[70:73], off offset:-2048 nt
	global_store_dwordx4 v[68:69], v[84:87], off offset:-2032 nt
	global_store_dwordx4 v[68:69], v[88:91], off nt
	global_store_dwordx4 v[68:69], v[92:95], off offset:16 nt
	v_lshl_add_u64 v[68:69], v[68:69], 0, s[4:5]
	s_cmp_lg_u32 s41, 0
	s_cbranch_scc1 .LBB0_1151
